# speedup vs baseline: 1.0051x; 1.0051x over previous
.Lk1_nowarm9:
	buffer_load_dword v8, v1, s[8:11], s40 offen nt
	buffer_load_dword v9, v1, s[8:11], s41 offen nt
	buffer_load_dword v10, v1, s[8:11], s42 offen nt
	buffer_load_dword v11, v1, s[8:11], s43 offen nt
	buffer_load_dword v12, v1, s[8:11], s44 offen nt
	buffer_load_dword v13, v1, s[8:11], s45 offen nt
	buffer_load_dword v14, v1, s[8:11], s46 offen nt
	buffer_load_dword v15, v1, s[8:11], s47 offen nt
	buffer_load_dword v16, v1, s[8:11], s48 offen nt
	buffer_load_dword v17, v1, s[8:11], s49 offen nt
	buffer_load_dword v18, v1, s[8:11], s50 offen nt
	buffer_load_dword v19, v1, s[8:11], s51 offen nt
	buffer_load_dword v20, v1, s[8:11], s52 offen nt
	buffer_load_dword v21, v1, s[8:11], s53 offen nt
	buffer_load_dword v22, v1, s[8:11], s54 offen nt
	buffer_load_dword v23, v1, s[8:11], s55 offen nt
	s_add_u32 s8, s8, 0x4e200
	s_addc_u32 s9, s9, 0
	buffer_load_dword v24, v1, s[8:11], s40 offen nt
	buffer_load_dword v25, v1, s[8:11], s41 offen nt
	buffer_load_dword v26, v1, s[8:11], s42 offen nt
	buffer_load_dword v27, v1, s[8:11], s43 offen nt
	buffer_load_dword v28, v1, s[8:11], s44 offen nt
	buffer_load_dword v29, v1, s[8:11], s45 offen nt
	buffer_load_dword v30, v1, s[8:11], s46 offen nt
	buffer_load_dword v31, v1, s[8:11], s47 offen nt
	buffer_load_dword v32, v1, s[8:11], s48 offen nt
	buffer_load_dword v33, v1, s[8:11], s49 offen nt
	buffer_load_dword v34, v1, s[8:11], s50 offen nt
	buffer_load_dword v35, v1, s[8:11], s51 offen nt
	buffer_load_dword v36, v1, s[8:11], s52 offen nt
	buffer_load_dword v37, v1, s[8:11], s53 offen nt
	buffer_load_dword v38, v1, s[8:11], s54 offen nt
	buffer_load_dword v39, v1, s[8:11], s55 offen nt
	s_add_u32 s8, s8, 0x4e200
	s_addc_u32 s9, s9, 0
	buffer_load_dword v40, v1, s[8:11], s40 offen nt
	buffer_load_dword v41, v1, s[8:11], s41 offen nt
	buffer_load_dword v42, v1, s[8:11], s42 offen nt
	buffer_load_dword v43, v1, s[8:11], s43 offen nt
	buffer_load_dword v44, v1, s[8:11], s44 offen nt
	buffer_load_dword v45, v1, s[8:11], s45 offen nt
	buffer_load_dword v46, v1, s[8:11], s46 offen nt
	buffer_load_dword v47, v1, s[8:11], s47 offen nt
	buffer_load_dword v48, v1, s[8:11], s48 offen nt
	buffer_load_dword v49, v1, s[8:11], s49 offen nt
	buffer_load_dword v50, v1, s[8:11], s50 offen nt
	buffer_load_dword v51, v1, s[8:11], s51 offen nt
	buffer_load_dword v52, v1, s[8:11], s52 offen nt
	buffer_load_dword v53, v1, s[8:11], s53 offen nt
	buffer_load_dword v54, v1, s[8:11], s54 offen nt
	buffer_load_dword v55, v1, s[8:11], s55 offen nt
	s_add_u32 s8, s8, 0x4e200
	s_addc_u32 s9, s9, 0
	buffer_load_dword v56, v1, s[8:11], s40 offen nt
	buffer_load_dword v57, v1, s[8:11], s41 offen nt
	buffer_load_dword v58, v1, s[8:11], s42 offen nt
	buffer_load_dword v59, v1, s[8:11], s43 offen nt
	buffer_load_dword v60, v1, s[8:11], s44 offen nt
	buffer_load_dword v61, v1, s[8:11], s45 offen nt
	buffer_load_dword v62, v1, s[8:11], s46 offen nt
	buffer_load_dword v63, v1, s[8:11], s47 offen nt
	buffer_load_dword v64, v1, s[8:11], s48 offen nt
	buffer_load_dword v65, v1, s[8:11], s49 offen nt
	buffer_load_dword v66, v1, s[8:11], s50 offen nt
	v_mul_u32_u24_e32 v3, 0x147b, v2
	v_lshrrev_b32_e32 v3, 19, v3
	v_mul_u32_u24_e32 v98, 0x64, v3
	v_sub_u32_e32 v98, v2, v98
	v_add_u32_e32 v3, -1, v3
	v_add_u32_e32 v98, -1, v98
	s_movk_i32 s17, 0x62
	v_cmp_gt_u32_e64 s[36:37], 48, v3
	v_cmp_gt_u32_e64 s[38:39], s17, v98
	s_mul_i32 s17, s15, 0x1388
	v_add_lshl_u32 v98, v2, s17, 3
	s_and_b64 s[36:37], s[36:37], s[38:39]
	s_waitcnt vmcnt(55)
	buffer_load_dword v67, v1, s[8:11], s51 offen nt
	buffer_load_dword v68, v1, s[8:11], s52 offen nt
	buffer_load_dword v69, v1, s[8:11], s53 offen nt
	buffer_load_dword v70, v1, s[8:11], s54 offen nt
	buffer_load_dword v71, v1, s[8:11], s55 offen nt
	s_add_u32 s8, s8, 0x4e200
	s_addc_u32 s9, s9, 0
	buffer_load_dword v72, v1, s[8:11], s40 offen nt
	s_waitcnt vmcnt(49)
	v_max3_f32 v76, v8, v9, v10
	v_max3_f32 v76, v76, v11, v12
	v_max3_f32 v76, v76, v13, v14
	v_max3_f32 v76, v76, v15, v16
	v_max3_f32 v76, v76, v17, v18
	v_max3_f32 v76, v76, v19, v20
	v_max3_f32 v76, v76, v21, v22
	v_max_f32_e32 v76, v76, v23
	v_pk_add_f32 v[8:9], v[8:9], v[76:77] op_sel_hi:[1,0] neg_lo:[0,1] neg_hi:[0,1]
	v_pk_add_f32 v[10:11], v[10:11], v[76:77] op_sel_hi:[1,0] neg_lo:[0,1] neg_hi:[0,1]
	v_pk_add_f32 v[12:13], v[12:13], v[76:77] op_sel_hi:[1,0] neg_lo:[0,1] neg_hi:[0,1]
	v_pk_add_f32 v[14:15], v[14:15], v[76:77] op_sel_hi:[1,0] neg_lo:[0,1] neg_hi:[0,1]
	v_pk_add_f32 v[16:17], v[16:17], v[76:77] op_sel_hi:[1,0] neg_lo:[0,1] neg_hi:[0,1]
	v_pk_add_f32 v[18:19], v[18:19], v[76:77] op_sel_hi:[1,0] neg_lo:[0,1] neg_hi:[0,1]
	v_pk_add_f32 v[20:21], v[20:21], v[76:77] op_sel_hi:[1,0] neg_lo:[0,1] neg_hi:[0,1]
	v_pk_add_f32 v[22:23], v[22:23], v[76:77] op_sel_hi:[1,0] neg_lo:[0,1] neg_hi:[0,1]
	v_or_b32_e32 v81, 0, v8
	v_or_b32_e32 v82, 1, v9
	v_min_u32_e32 v80, v81, v82
	v_or_b32_e32 v81, 2, v10
	v_or_b32_e32 v82, 3, v11
	v_min3_u32 v80, v80, v81, v82
	v_or_b32_e32 v81, 4, v12
	v_or_b32_e32 v82, 5, v13
	v_min3_u32 v80, v80, v81, v82
	v_or_b32_e32 v81, 6, v14
	v_or_b32_e32 v82, 7, v15
	v_min3_u32 v80, v80, v81, v82
	v_or_b32_e32 v81, 8, v16
	v_or_b32_e32 v82, 9, v17
	v_min3_u32 v80, v80, v81, v82
	v_or_b32_e32 v81, 10, v18
	v_or_b32_e32 v82, 11, v19
	v_min3_u32 v80, v80, v81, v82
	v_or_b32_e32 v81, 12, v20
	v_or_b32_e32 v82, 13, v21
	v_min3_u32 v80, v80, v81, v82
	v_or_b32_e32 v81, 14, v22
	v_or_b32_e32 v82, 15, v23
	v_min3_u32 v80, v80, v81, v82
	v_pk_mul_f32 v[8:9], v[8:9], s[14:15] op_sel_hi:[1,0]
	v_pk_mul_f32 v[10:11], v[10:11], s[14:15] op_sel_hi:[1,0]
	v_pk_mul_f32 v[12:13], v[12:13], s[14:15] op_sel_hi:[1,0]
	v_pk_mul_f32 v[14:15], v[14:15], s[14:15] op_sel_hi:[1,0]
	v_pk_mul_f32 v[16:17], v[16:17], s[14:15] op_sel_hi:[1,0]
	v_pk_mul_f32 v[18:19], v[18:19], s[14:15] op_sel_hi:[1,0]
	v_pk_mul_f32 v[20:21], v[20:21], s[14:15] op_sel_hi:[1,0]
	v_pk_mul_f32 v[22:23], v[22:23], s[14:15] op_sel_hi:[1,0]
	v_exp_f32_e32 v8, v8
	v_exp_f32_e32 v9, v9
	v_exp_f32_e32 v10, v10
	v_exp_f32_e32 v11, v11
	v_exp_f32_e32 v12, v12
	v_exp_f32_e32 v13, v13
	v_exp_f32_e32 v14, v14
	v_exp_f32_e32 v15, v15
	v_exp_f32_e32 v16, v16
	v_exp_f32_e32 v17, v17
	v_exp_f32_e32 v18, v18
	v_exp_f32_e32 v19, v19
	v_exp_f32_e32 v20, v20
	v_exp_f32_e32 v21, v21
	v_exp_f32_e32 v22, v22
	v_exp_f32_e32 v23, v23
	v_pk_add_f32 v[78:79], v[8:9], v[10:11]
	v_pk_add_f32 v[78:79], v[78:79], v[12:13]
	v_pk_add_f32 v[78:79], v[78:79], v[14:15]
	v_pk_add_f32 v[78:79], v[78:79], v[16:17]
	v_pk_add_f32 v[78:79], v[78:79], v[18:19]
	v_pk_add_f32 v[78:79], v[78:79], v[20:21]
	v_pk_add_f32 v[78:79], v[78:79], v[22:23]
	v_add_f32_e32 v78, v78, v79
	v_cvt_f64_f32_e32 v[86:87], v78
	v_mov_b32_e32 v75, v80
	v_mov_b32_e32 v73, v76
	s_waitcnt vmcnt(33)
	v_max3_f32 v76, v24, v25, v26
	v_max3_f32 v76, v76, v27, v28
	v_max3_f32 v76, v76, v29, v30
	v_max3_f32 v76, v76, v31, v32
	v_max3_f32 v76, v76, v33, v34
	v_max3_f32 v76, v76, v35, v36
	v_max3_f32 v76, v76, v37, v38
	v_max_f32_e32 v76, v76, v39
	v_max_f32_e32 v100, v73, v76
	v_cmp_gt_f32_e64 s[26:27], v76, v73
	v_sub_f32_e32 v83, v73, v100
	v_mul_f32_e32 v83, s14, v83
	v_exp_f32_e32 v83, v83
	v_pk_add_f32 v[24:25], v[24:25], v[100:101] op_sel_hi:[1,0] neg_lo:[0,1] neg_hi:[0,1]
	v_pk_add_f32 v[26:27], v[26:27], v[100:101] op_sel_hi:[1,0] neg_lo:[0,1] neg_hi:[0,1]
	v_pk_add_f32 v[28:29], v[28:29], v[100:101] op_sel_hi:[1,0] neg_lo:[0,1] neg_hi:[0,1]
	v_pk_add_f32 v[30:31], v[30:31], v[100:101] op_sel_hi:[1,0] neg_lo:[0,1] neg_hi:[0,1]
	v_pk_add_f32 v[32:33], v[32:33], v[100:101] op_sel_hi:[1,0] neg_lo:[0,1] neg_hi:[0,1]
	v_pk_add_f32 v[34:35], v[34:35], v[100:101] op_sel_hi:[1,0] neg_lo:[0,1] neg_hi:[0,1]
	v_pk_add_f32 v[36:37], v[36:37], v[100:101] op_sel_hi:[1,0] neg_lo:[0,1] neg_hi:[0,1]
	v_pk_add_f32 v[38:39], v[38:39], v[100:101] op_sel_hi:[1,0] neg_lo:[0,1] neg_hi:[0,1]
	v_cvt_f64_f32_e32 v[90:91], v83
	v_or_b32_e32 v81, 16, v24
	v_or_b32_e32 v82, 17, v25
	v_min_u32_e32 v80, v81, v82
	v_or_b32_e32 v81, 18, v26
	v_or_b32_e32 v82, 19, v27
	v_min3_u32 v80, v80, v81, v82
	v_or_b32_e32 v81, 20, v28
	v_or_b32_e32 v82, 21, v29
	v_min3_u32 v80, v80, v81, v82
	v_or_b32_e32 v81, 22, v30
	v_or_b32_e32 v82, 23, v31
	v_min3_u32 v80, v80, v81, v82
	v_or_b32_e32 v81, 24, v32
	v_or_b32_e32 v82, 25, v33
	v_min3_u32 v80, v80, v81, v82
	v_or_b32_e32 v81, 26, v34
	v_or_b32_e32 v82, 27, v35
	v_min3_u32 v80, v80, v81, v82
	v_or_b32_e32 v81, 28, v36
	v_or_b32_e32 v82, 29, v37
	v_min3_u32 v80, v80, v81, v82
	v_or_b32_e32 v81, 30, v38
	v_or_b32_e32 v82, 31, v39
	v_min3_u32 v80, v80, v81, v82
	v_pk_mul_f32 v[24:25], v[24:25], s[14:15] op_sel_hi:[1,0]
	v_pk_mul_f32 v[26:27], v[26:27], s[14:15] op_sel_hi:[1,0]
	v_pk_mul_f32 v[28:29], v[28:29], s[14:15] op_sel_hi:[1,0]
	v_pk_mul_f32 v[30:31], v[30:31], s[14:15] op_sel_hi:[1,0]
	v_pk_mul_f32 v[32:33], v[32:33], s[14:15] op_sel_hi:[1,0]
	v_pk_mul_f32 v[34:35], v[34:35], s[14:15] op_sel_hi:[1,0]
	v_pk_mul_f32 v[36:37], v[36:37], s[14:15] op_sel_hi:[1,0]
	v_pk_mul_f32 v[38:39], v[38:39], s[14:15] op_sel_hi:[1,0]
	v_exp_f32_e32 v24, v24
	v_exp_f32_e32 v25, v25
	v_exp_f32_e32 v26, v26
	v_exp_f32_e32 v27, v27
	v_exp_f32_e32 v28, v28
	v_exp_f32_e32 v29, v29
	v_exp_f32_e32 v30, v30
	v_exp_f32_e32 v31, v31
	v_exp_f32_e32 v32, v32
	v_exp_f32_e32 v33, v33
	v_exp_f32_e32 v34, v34
	v_exp_f32_e32 v35, v35
	v_exp_f32_e32 v36, v36
	v_exp_f32_e32 v37, v37
	v_exp_f32_e32 v38, v38
	v_exp_f32_e32 v39, v39
	v_pk_add_f32 v[78:79], v[24:25], v[26:27]
	v_pk_add_f32 v[78:79], v[78:79], v[28:29]
	v_pk_add_f32 v[78:79], v[78:79], v[30:31]
	v_pk_add_f32 v[78:79], v[78:79], v[32:33]
	v_pk_add_f32 v[78:79], v[78:79], v[34:35]
	v_pk_add_f32 v[78:79], v[78:79], v[36:37]
	v_pk_add_f32 v[78:79], v[78:79], v[38:39]
	v_add_f32_e32 v78, v78, v79
	v_cvt_f64_f32_e32 v[84:85], v78
	v_cndmask_b32_e64 v75, v75, v80, s[26:27]
	v_mov_b32_e32 v73, v100
	v_fma_f64 v[86:87], v[86:87], v[90:91], v[84:85]
	s_waitcnt vmcnt(17)
	v_max3_f32 v76, v40, v41, v42
	v_max3_f32 v76, v76, v43, v44
	v_max3_f32 v76, v76, v45, v46
	v_max3_f32 v76, v76, v47, v48
	v_max3_f32 v76, v76, v49, v50
	v_max3_f32 v76, v76, v51, v52
	v_max3_f32 v76, v76, v53, v54
	v_max_f32_e32 v76, v76, v55
	v_max_f32_e32 v100, v73, v76
	v_cmp_gt_f32_e64 s[26:27], v76, v73
	v_sub_f32_e32 v83, v73, v100
	v_mul_f32_e32 v83, s14, v83
	v_exp_f32_e32 v83, v83
	v_pk_add_f32 v[40:41], v[40:41], v[100:101] op_sel_hi:[1,0] neg_lo:[0,1] neg_hi:[0,1]
	v_pk_add_f32 v[42:43], v[42:43], v[100:101] op_sel_hi:[1,0] neg_lo:[0,1] neg_hi:[0,1]
	v_pk_add_f32 v[44:45], v[44:45], v[100:101] op_sel_hi:[1,0] neg_lo:[0,1] neg_hi:[0,1]
	v_pk_add_f32 v[46:47], v[46:47], v[100:101] op_sel_hi:[1,0] neg_lo:[0,1] neg_hi:[0,1]
	v_pk_add_f32 v[48:49], v[48:49], v[100:101] op_sel_hi:[1,0] neg_lo:[0,1] neg_hi:[0,1]
	v_pk_add_f32 v[50:51], v[50:51], v[100:101] op_sel_hi:[1,0] neg_lo:[0,1] neg_hi:[0,1]
	v_pk_add_f32 v[52:53], v[52:53], v[100:101] op_sel_hi:[1,0] neg_lo:[0,1] neg_hi:[0,1]
	v_pk_add_f32 v[54:55], v[54:55], v[100:101] op_sel_hi:[1,0] neg_lo:[0,1] neg_hi:[0,1]
	v_cvt_f64_f32_e32 v[90:91], v83
	v_or_b32_e32 v81, 32, v40
	v_or_b32_e32 v82, 33, v41
	v_min_u32_e32 v80, v81, v82
	v_or_b32_e32 v81, 34, v42
	v_or_b32_e32 v82, 35, v43
	v_min3_u32 v80, v80, v81, v82
	v_or_b32_e32 v81, 36, v44
	v_or_b32_e32 v82, 37, v45
	v_min3_u32 v80, v80, v81, v82
	v_or_b32_e32 v81, 38, v46
	v_or_b32_e32 v82, 39, v47
	v_min3_u32 v80, v80, v81, v82
	v_or_b32_e32 v81, 40, v48
	v_or_b32_e32 v82, 41, v49
	v_min3_u32 v80, v80, v81, v82
	v_or_b32_e32 v81, 42, v50
	v_or_b32_e32 v82, 43, v51
	v_min3_u32 v80, v80, v81, v82
	v_or_b32_e32 v81, 44, v52
	v_or_b32_e32 v82, 45, v53
	v_min3_u32 v80, v80, v81, v82
	v_or_b32_e32 v81, 46, v54
	v_or_b32_e32 v82, 47, v55
	v_min3_u32 v80, v80, v81, v82
	v_pk_mul_f32 v[40:41], v[40:41], s[14:15] op_sel_hi:[1,0]
	v_pk_mul_f32 v[42:43], v[42:43], s[14:15] op_sel_hi:[1,0]
	v_pk_mul_f32 v[44:45], v[44:45], s[14:15] op_sel_hi:[1,0]
	v_pk_mul_f32 v[46:47], v[46:47], s[14:15] op_sel_hi:[1,0]
	v_pk_mul_f32 v[48:49], v[48:49], s[14:15] op_sel_hi:[1,0]
	v_pk_mul_f32 v[50:51], v[50:51], s[14:15] op_sel_hi:[1,0]
	v_pk_mul_f32 v[52:53], v[52:53], s[14:15] op_sel_hi:[1,0]
	v_pk_mul_f32 v[54:55], v[54:55], s[14:15] op_sel_hi:[1,0]
	v_exp_f32_e32 v40, v40
	v_exp_f32_e32 v41, v41
	v_exp_f32_e32 v42, v42
	v_exp_f32_e32 v43, v43
	v_exp_f32_e32 v44, v44
	v_exp_f32_e32 v45, v45
	v_exp_f32_e32 v46, v46
	v_exp_f32_e32 v47, v47
	v_exp_f32_e32 v48, v48
	v_exp_f32_e32 v49, v49
	v_exp_f32_e32 v50, v50
	v_exp_f32_e32 v51, v51
	v_exp_f32_e32 v52, v52
	v_exp_f32_e32 v53, v53
	v_exp_f32_e32 v54, v54
	v_exp_f32_e32 v55, v55
	v_pk_add_f32 v[78:79], v[40:41], v[42:43]
	v_pk_add_f32 v[78:79], v[78:79], v[44:45]
	v_pk_add_f32 v[78:79], v[78:79], v[46:47]
	v_pk_add_f32 v[78:79], v[78:79], v[48:49]
	v_pk_add_f32 v[78:79], v[78:79], v[50:51]
	v_pk_add_f32 v[78:79], v[78:79], v[52:53]
	v_pk_add_f32 v[78:79], v[78:79], v[54:55]
	v_add_f32_e32 v78, v78, v79
	v_cvt_f64_f32_e32 v[84:85], v78
	v_cndmask_b32_e64 v75, v75, v80, s[26:27]
	v_mov_b32_e32 v73, v100
	v_fma_f64 v[86:87], v[86:87], v[90:91], v[84:85]
	s_waitcnt vmcnt(9)
	v_max3_f32 v76, v56, v57, v58
	v_max3_f32 v76, v76, v59, v60
	v_max3_f32 v76, v76, v61, v62
	v_max_f32_e32 v76, v76, v63
	v_max_f32_e32 v100, v73, v76
	v_cmp_gt_f32_e64 s[26:27], v76, v73
	v_sub_f32_e32 v83, v73, v100
	v_mul_f32_e32 v83, s14, v83
	v_exp_f32_e32 v83, v83
	v_pk_add_f32 v[56:57], v[56:57], v[100:101] op_sel_hi:[1,0] neg_lo:[0,1] neg_hi:[0,1]
	v_pk_add_f32 v[58:59], v[58:59], v[100:101] op_sel_hi:[1,0] neg_lo:[0,1] neg_hi:[0,1]
	v_pk_add_f32 v[60:61], v[60:61], v[100:101] op_sel_hi:[1,0] neg_lo:[0,1] neg_hi:[0,1]
	v_pk_add_f32 v[62:63], v[62:63], v[100:101] op_sel_hi:[1,0] neg_lo:[0,1] neg_hi:[0,1]
	v_cvt_f64_f32_e32 v[90:91], v83
	v_or_b32_e32 v81, 48, v56
	v_or_b32_e32 v82, 49, v57
	v_min_u32_e32 v80, v81, v82
	v_or_b32_e32 v81, 50, v58
	v_or_b32_e32 v82, 51, v59
	v_min3_u32 v80, v80, v81, v82
	v_or_b32_e32 v81, 52, v60
	v_or_b32_e32 v82, 53, v61
	v_min3_u32 v80, v80, v81, v82
	v_or_b32_e32 v81, 54, v62
	v_or_b32_e32 v82, 55, v63
	v_min3_u32 v80, v80, v81, v82
	v_pk_mul_f32 v[56:57], v[56:57], s[14:15] op_sel_hi:[1,0]
	v_pk_mul_f32 v[58:59], v[58:59], s[14:15] op_sel_hi:[1,0]
	v_pk_mul_f32 v[60:61], v[60:61], s[14:15] op_sel_hi:[1,0]
	v_pk_mul_f32 v[62:63], v[62:63], s[14:15] op_sel_hi:[1,0]
	v_exp_f32_e32 v56, v56
	v_exp_f32_e32 v57, v57
	v_exp_f32_e32 v58, v58
	v_exp_f32_e32 v59, v59
	v_exp_f32_e32 v60, v60
	v_exp_f32_e32 v61, v61
	v_exp_f32_e32 v62, v62
	v_exp_f32_e32 v63, v63
	v_pk_add_f32 v[78:79], v[56:57], v[58:59]
	v_pk_add_f32 v[78:79], v[78:79], v[60:61]
	v_pk_add_f32 v[78:79], v[78:79], v[62:63]
	v_add_f32_e32 v78, v78, v79
	v_cvt_f64_f32_e32 v[84:85], v78
	v_cndmask_b32_e64 v75, v75, v80, s[26:27]
	v_mov_b32_e32 v73, v100
	v_fma_f64 v[86:87], v[86:87], v[90:91], v[84:85]
	s_waitcnt vmcnt(5)
	v_max3_f32 v76, v64, v65, v66
	v_max_f32_e32 v76, v76, v67
	v_max_f32_e32 v100, v73, v76
	v_cmp_gt_f32_e64 s[26:27], v76, v73
	v_sub_f32_e32 v83, v73, v100
	v_mul_f32_e32 v83, s14, v83
	v_exp_f32_e32 v83, v83
	v_pk_add_f32 v[64:65], v[64:65], v[100:101] op_sel_hi:[1,0] neg_lo:[0,1] neg_hi:[0,1]
	v_pk_add_f32 v[66:67], v[66:67], v[100:101] op_sel_hi:[1,0] neg_lo:[0,1] neg_hi:[0,1]
	v_cvt_f64_f32_e32 v[90:91], v83
	v_or_b32_e32 v81, 56, v64
	v_or_b32_e32 v82, 57, v65
	v_min_u32_e32 v80, v81, v82
	v_or_b32_e32 v81, 58, v66
	v_or_b32_e32 v82, 59, v67
	v_min3_u32 v80, v80, v81, v82
	v_pk_mul_f32 v[64:65], v[64:65], s[14:15] op_sel_hi:[1,0]
	v_pk_mul_f32 v[66:67], v[66:67], s[14:15] op_sel_hi:[1,0]
	v_exp_f32_e32 v64, v64
	v_exp_f32_e32 v65, v65
	v_exp_f32_e32 v66, v66
	v_exp_f32_e32 v67, v67
	s_nop 0
	v_pk_add_f32 v[78:79], v[64:65], v[66:67]
	v_add_f32_e32 v78, v78, v79
	v_cvt_f64_f32_e32 v[84:85], v78
	v_cndmask_b32_e64 v75, v75, v80, s[26:27]
	v_mov_b32_e32 v73, v100
	v_fma_f64 v[86:87], v[86:87], v[90:91], v[84:85]
	s_waitcnt vmcnt(0)
	v_max3_f32 v76, v68, v69, v70
	v_max3_f32 v76, v76, v71, v72
	v_max_f32_e32 v100, v73, v76
	v_cmp_gt_f32_e64 s[26:27], v76, v73
	v_sub_f32_e32 v83, v73, v100
	v_mul_f32_e32 v83, s14, v83
	v_exp_f32_e32 v83, v83
	v_pk_add_f32 v[68:69], v[68:69], v[100:101] op_sel_hi:[1,0] neg_lo:[0,1] neg_hi:[0,1]
	v_pk_add_f32 v[70:71], v[70:71], v[100:101] op_sel_hi:[1,0] neg_lo:[0,1] neg_hi:[0,1]
	v_sub_f32_e32 v72, v72, v100
	v_cvt_f64_f32_e32 v[90:91], v83
	v_or_b32_e32 v81, 60, v68
	v_or_b32_e32 v82, 61, v69
	v_min_u32_e32 v80, v81, v82
	v_or_b32_e32 v81, 62, v70
	v_or_b32_e32 v82, 63, v71
	v_min3_u32 v80, v80, v81, v82
	v_or_b32_e32 v81, 64, v72
	v_min_u32_e32 v80, v80, v81
	v_pk_mul_f32 v[68:69], v[68:69], s[14:15] op_sel_hi:[1,0]
	v_pk_mul_f32 v[70:71], v[70:71], s[14:15] op_sel_hi:[1,0]
	v_mul_f32_e32 v72, s14, v72
	v_exp_f32_e32 v68, v68
	v_exp_f32_e32 v69, v69
	v_exp_f32_e32 v70, v70
	v_exp_f32_e32 v71, v71
	v_exp_f32_e32 v72, v72
	v_cndmask_b32_e64 v75, v75, v80, s[26:27]
	v_pk_add_f32 v[78:79], v[68:69], v[70:71]
	v_add_f32_e32 v78, v78, v79
	v_add_f32_e32 v78, v78, v72
	v_cvt_f64_f32_e32 v[84:85], v78
	v_fma_f64 v[86:87], v[86:87], v[90:91], v[84:85]
	v_rcp_f64_e32 v[88:89], v[86:87]
	v_cmp_gt_u32_e32 vcc, 64, v75
	s_and_b64 vcc, vcc, s[36:37]
	v_fma_f64 v[90:91], -v[86:87], v[88:89], 1.0
	v_fma_f64 v[88:89], v[90:91], v[88:89], v[88:89]
	v_cvt_f32_f64_e32 v3, v[88:89]
	v_cndmask_b32_e32 v74, 0, v3, vcc
	global_store_dwordx2 v98, v[74:75], s[6:7]
